# baseline (speedup 1.0000x reference)
.Lsched_scan:
	s_add_u32 s55, s53, s54
	s_and_b32 s55, s55, 7
	s_lshl_b32 s0, s55, 2
	s_add_u32 s1, s76, s0
	v_mov_b32_e32 v2, s1
	ds_read_b32 v2, v2 offset:32
	s_waitcnt lgkmcnt(0)
	v_readfirstlane_b32 s33, v2
	s_mul_i32 s34, s33, 17
	s_addk_i32 s34, 0x50
	s_cmp_eq_u32 s54, 0
	s_cbranch_scc1 .Lsched_have_h
	s_cmp_lg_u32 s54, 1
	s_cbranch_scc1 .Lsched_snapped
	s_mov_b64 exec, 0xff
	v_mbcnt_lo_u32_b32 v5, -1, 0
	v_lshlrev_b32_e32 v5, 2, v5
	global_load_dword v5, v5, s[56:57] sc1
	s_waitcnt vmcnt(0)
	s_mov_b64 exec, 1
.Lsched_snapped:
	s_nop 1
	v_readlane_b32 s1, v5, s55
	s_cmp_ge_i32 s1, s34
	s_cbranch_scc1 .Lsched_next
	v_mov_b32_e32 v2, s0
	v_mov_b32_e32 v3, 1
	global_atomic_add v3, v2, v3, s[56:57] sc0
	s_waitcnt vmcnt(0)
	v_readfirstlane_b32 s52, v3

.LBB2_286:
	s_or_b64 exec, exec, s[2:3]
	v_ashrrev_i32_e32 v130, 6, v4
	v_lshl_add_u32 v6, v130, 5, 0
	v_lshlrev_b32_e32 v2, 3, v4
	s_barrier
	v_and_b32_e32 v134, 0x1f8, v2
	ds_read_b128 v[2:5], v6
	ds_read_b128 v[6:9], v6 offset:16
	v_readlane_b32 s2, v244, 0
	v_lshlrev_b32_e32 v162, 1, v134
	v_readlane_b32 s3, v244, 1
	s_waitcnt lgkmcnt(1)
	v_ashrrev_i32_e32 v13, 31, v2
	v_mov_b32_e32 v12, v2
	v_lshl_add_u64 v[10:11], s[2:3], 0, v[162:163]
	v_ashrrev_i32_e32 v15, 31, v3
	v_mov_b32_e32 v14, v3
	v_lshlrev_b64 v[12:13], 12, v[12:13]
	v_lshlrev_b64 v[2:3], 12, v[14:15]
	v_lshl_add_u64 v[12:13], v[10:11], 0, v[12:13]
	v_lshl_add_u64 v[2:3], v[10:11], 0, v[2:3]
	global_load_dwordx4 v[122:125], v[12:13], off
	global_load_dwordx4 v[126:129], v[2:3], off
	global_load_dwordx4 v[118:121], v[12:13], off offset:1024
	global_load_dwordx4 v[114:117], v[2:3], off offset:1024
	global_load_dwordx4 v[110:113], v[12:13], off offset:2048
	global_load_dwordx4 v[106:109], v[2:3], off offset:2048
	global_load_dwordx4 v[102:105], v[12:13], off offset:3072
	global_load_dwordx4 v[98:101], v[2:3], off offset:3072
	v_ashrrev_i32_e32 v3, 31, v4
	v_mov_b32_e32 v2, v4
	v_ashrrev_i32_e32 v13, 31, v5
	v_mov_b32_e32 v12, v5
	v_lshlrev_b64 v[2:3], 12, v[2:3]
	v_lshlrev_b64 v[4:5], 12, v[12:13]
	v_lshl_add_u64 v[2:3], v[10:11], 0, v[2:3]
	v_lshl_add_u64 v[4:5], v[10:11], 0, v[4:5]
	global_load_dwordx4 v[94:97], v[2:3], off
	global_load_dwordx4 v[90:93], v[4:5], off
	global_load_dwordx4 v[86:89], v[2:3], off offset:1024
	global_load_dwordx4 v[82:85], v[4:5], off offset:1024
	global_load_dwordx4 v[78:81], v[2:3], off offset:2048
	global_load_dwordx4 v[74:77], v[4:5], off offset:2048
	global_load_dwordx4 v[70:73], v[2:3], off offset:3072
	global_load_dwordx4 v[66:69], v[4:5], off offset:3072
	s_waitcnt lgkmcnt(0)
	v_ashrrev_i32_e32 v3, 31, v6
	v_mov_b32_e32 v2, v6
	v_ashrrev_i32_e32 v5, 31, v7
	v_mov_b32_e32 v4, v7
	v_lshlrev_b64 v[2:3], 12, v[2:3]
	s_lshl_b32 s2, s55, 5
	v_lshlrev_b64 v[4:5], 12, v[4:5]
	v_lshl_add_u64 v[2:3], v[10:11], 0, v[2:3]
	v_lshl_add_u32 v130, v130, 2, s2
	v_lshl_add_u64 v[4:5], v[10:11], 0, v[4:5]
	global_load_dwordx4 v[62:65], v[2:3], off
	global_load_dwordx4 v[58:61], v[4:5], off
	global_load_dwordx4 v[54:57], v[2:3], off offset:1024
	global_load_dwordx4 v[50:53], v[4:5], off offset:1024
	global_load_dwordx4 v[46:49], v[2:3], off offset:2048
	global_load_dwordx4 v[42:45], v[4:5], off offset:2048
	global_load_dwordx4 v[38:41], v[2:3], off offset:3072
	global_load_dwordx4 v[34:37], v[4:5], off offset:3072
	v_ashrrev_i32_e32 v131, 31, v130
	v_readlane_b32 s56, v244, 2
	v_ashrrev_i32_e32 v3, 31, v8
	v_mov_b32_e32 v2, v8
	v_ashrrev_i32_e32 v5, 31, v9
	v_mov_b32_e32 v4, v9
	v_lshlrev_b64 v[132:133], 13, v[130:131]
	v_readlane_b32 s58, v244, 4
	v_readlane_b32 s59, v244, 5
	v_lshlrev_b64 v[4:5], 12, v[4:5]
	v_lshlrev_b64 v[2:3], 12, v[2:3]
	v_lshlrev_b32_e32 v162, 2, v134
	v_lshl_add_u64 v[2:3], v[10:11], 0, v[2:3]
	v_lshl_add_u64 v[4:5], v[10:11], 0, v[4:5]
	global_load_dwordx4 v[30:33], v[2:3], off
	global_load_dwordx4 v[26:29], v[4:5], off
	global_load_dwordx4 v[22:25], v[2:3], off offset:1024
	global_load_dwordx4 v[18:21], v[4:5], off offset:1024
	global_load_dwordx4 v[14:17], v[2:3], off offset:2048
	global_load_dwordx4 v[10:13], v[4:5], off offset:2048
	global_load_dwordx4 v[6:9], v[2:3], off offset:3072
	s_nop 0
	global_load_dwordx4 v[2:5], v[4:5], off offset:3072
	s_movk_i32 s2, 0x1000
	s_mov_b64 s[4:5], 0x1000
	s_mov_b64 s[10:11], 0x1800
	v_readlane_b32 s57, v244, 3
	s_waitcnt vmcnt(31)
	v_cvt_f32_f16_e32 v136, v122
	v_cvt_f32_f16_sdwa v137, v122 dst_sel:DWORD dst_unused:UNUSED_PAD src0_sel:WORD_1
	s_waitcnt vmcnt(30)
	v_cvt_f32_f16_e32 v138, v126
	v_cvt_f32_f16_sdwa v139, v126 dst_sel:DWORD dst_unused:UNUSED_PAD src0_sel:WORD_1
	v_cvt_f32_f16_e32 v122, v123
	v_cvt_f32_f16_sdwa v123, v123 dst_sel:DWORD dst_unused:UNUSED_PAD src0_sel:WORD_1
	v_cvt_f32_f16_e32 v126, v127
	v_cvt_f32_f16_sdwa v127, v127 dst_sel:DWORD dst_unused:UNUSED_PAD src0_sel:WORD_1
	v_pk_add_f32 v[136:137], v[136:137], v[138:139]
	v_pk_add_f32 v[138:139], v[122:123], v[126:127]
	v_cvt_f32_f16_e32 v122, v124
	v_cvt_f32_f16_sdwa v123, v124 dst_sel:DWORD dst_unused:UNUSED_PAD src0_sel:WORD_1
	v_cvt_f32_f16_e32 v126, v128
	v_cvt_f32_f16_sdwa v127, v128 dst_sel:DWORD dst_unused:UNUSED_PAD src0_sel:WORD_1
	v_cvt_f32_f16_e32 v124, v125
	v_cvt_f32_f16_sdwa v125, v125 dst_sel:DWORD dst_unused:UNUSED_PAD src0_sel:WORD_1
	v_cvt_f32_f16_e32 v128, v129
	v_cvt_f32_f16_sdwa v129, v129 dst_sel:DWORD dst_unused:UNUSED_PAD src0_sel:WORD_1
	v_pk_add_f32 v[122:123], v[122:123], v[126:127]
	v_lshl_add_u64 v[126:127], s[58:59], 0, v[132:133]
	v_lshl_add_u64 v[126:127], v[126:127], 0, v[162:163]
	v_pk_add_f32 v[124:125], v[124:125], v[128:129]
	global_store_dwordx4 v[126:127], v[136:139], off nt
	global_store_dwordx4 v[126:127], v[122:125], off offset:16 nt
	s_waitcnt vmcnt(31)
	s_nop 0
	v_cvt_f32_f16_e32 v122, v118
	v_cvt_f32_f16_sdwa v123, v118 dst_sel:DWORD dst_unused:UNUSED_PAD src0_sel:WORD_1
	s_waitcnt vmcnt(30)
	v_cvt_f32_f16_e32 v124, v114
	v_cvt_f32_f16_sdwa v125, v114 dst_sel:DWORD dst_unused:UNUSED_PAD src0_sel:WORD_1
	v_cvt_f32_f16_e32 v118, v119
	v_cvt_f32_f16_sdwa v119, v119 dst_sel:DWORD dst_unused:UNUSED_PAD src0_sel:WORD_1
	v_cvt_f32_f16_e32 v114, v115
	v_cvt_f32_f16_sdwa v115, v115 dst_sel:DWORD dst_unused:UNUSED_PAD src0_sel:WORD_1
	v_pk_add_f32 v[122:123], v[122:123], v[124:125]
	v_pk_add_f32 v[124:125], v[118:119], v[114:115]
	v_cvt_f32_f16_e32 v114, v120
	v_cvt_f32_f16_sdwa v115, v120 dst_sel:DWORD dst_unused:UNUSED_PAD src0_sel:WORD_1
	v_cvt_f32_f16_e32 v118, v116
	v_cvt_f32_f16_sdwa v119, v116 dst_sel:DWORD dst_unused:UNUSED_PAD src0_sel:WORD_1
	v_cvt_f32_f16_e32 v120, v121
	v_cvt_f32_f16_sdwa v121, v121 dst_sel:DWORD dst_unused:UNUSED_PAD src0_sel:WORD_1
	v_cvt_f32_f16_e32 v116, v117
	v_cvt_f32_f16_sdwa v117, v117 dst_sel:DWORD dst_unused:UNUSED_PAD src0_sel:WORD_1
	v_pk_add_f32 v[114:115], v[114:115], v[118:119]
	v_pk_add_f32 v[116:117], v[120:121], v[116:117]
	global_store_dwordx4 v[126:127], v[122:125], off offset:2048 nt
	global_store_dwordx4 v[126:127], v[114:117], off offset:2064 nt
	s_waitcnt vmcnt(31)
	s_nop 0
	v_cvt_f32_f16_e32 v114, v110
	v_cvt_f32_f16_sdwa v115, v110 dst_sel:DWORD dst_unused:UNUSED_PAD src0_sel:WORD_1
	s_waitcnt vmcnt(30)
	v_cvt_f32_f16_e32 v116, v106
	v_cvt_f32_f16_sdwa v117, v106 dst_sel:DWORD dst_unused:UNUSED_PAD src0_sel:WORD_1
	v_cvt_f32_f16_e32 v110, v111
	v_cvt_f32_f16_sdwa v111, v111 dst_sel:DWORD dst_unused:UNUSED_PAD src0_sel:WORD_1
	v_cvt_f32_f16_e32 v106, v107
	v_cvt_f32_f16_sdwa v107, v107 dst_sel:DWORD dst_unused:UNUSED_PAD src0_sel:WORD_1
	v_pk_add_f32 v[114:115], v[114:115], v[116:117]
	v_pk_add_f32 v[116:117], v[110:111], v[106:107]
	v_cvt_f32_f16_e32 v106, v112
	v_cvt_f32_f16_sdwa v107, v112 dst_sel:DWORD dst_unused:UNUSED_PAD src0_sel:WORD_1
	v_cvt_f32_f16_e32 v110, v108
	v_cvt_f32_f16_sdwa v111, v108 dst_sel:DWORD dst_unused:UNUSED_PAD src0_sel:WORD_1
	v_cvt_f32_f16_e32 v112, v113
	v_cvt_f32_f16_sdwa v113, v113 dst_sel:DWORD dst_unused:UNUSED_PAD src0_sel:WORD_1
	v_cvt_f32_f16_e32 v108, v109
	v_cvt_f32_f16_sdwa v109, v109 dst_sel:DWORD dst_unused:UNUSED_PAD src0_sel:WORD_1
	v_pk_add_f32 v[106:107], v[106:107], v[110:111]
	v_lshl_add_u64 v[110:111], v[126:127], 0, s[4:5]
	v_pk_add_f32 v[108:109], v[112:113], v[108:109]
	v_add_co_u32_e32 v112, vcc, s2, v126
	s_nop 1
	v_addc_co_u32_e32 v113, vcc, 0, v127, vcc
	global_store_dwordx4 v[112:113], v[114:117], off nt
	global_store_dwordx4 v[110:111], v[106:109], off offset:16 nt
	s_waitcnt vmcnt(31)
	s_nop 0
	v_cvt_f32_f16_e32 v106, v102
	v_cvt_f32_f16_sdwa v107, v102 dst_sel:DWORD dst_unused:UNUSED_PAD src0_sel:WORD_1
	s_waitcnt vmcnt(30)
	v_cvt_f32_f16_e32 v108, v98
	v_cvt_f32_f16_sdwa v109, v98 dst_sel:DWORD dst_unused:UNUSED_PAD src0_sel:WORD_1
	v_cvt_f32_f16_e32 v102, v103
	v_cvt_f32_f16_sdwa v103, v103 dst_sel:DWORD dst_unused:UNUSED_PAD src0_sel:WORD_1
	v_cvt_f32_f16_e32 v98, v99
	v_cvt_f32_f16_sdwa v99, v99 dst_sel:DWORD dst_unused:UNUSED_PAD src0_sel:WORD_1
	v_pk_add_f32 v[106:107], v[106:107], v[108:109]
	v_pk_add_f32 v[108:109], v[102:103], v[98:99]
	v_cvt_f32_f16_e32 v98, v104
	v_cvt_f32_f16_sdwa v99, v104 dst_sel:DWORD dst_unused:UNUSED_PAD src0_sel:WORD_1
	v_cvt_f32_f16_e32 v102, v100
	v_cvt_f32_f16_sdwa v103, v100 dst_sel:DWORD dst_unused:UNUSED_PAD src0_sel:WORD_1
	v_cvt_f32_f16_e32 v104, v105
	v_cvt_f32_f16_sdwa v105, v105 dst_sel:DWORD dst_unused:UNUSED_PAD src0_sel:WORD_1
	v_cvt_f32_f16_e32 v100, v101
	v_cvt_f32_f16_sdwa v101, v101 dst_sel:DWORD dst_unused:UNUSED_PAD src0_sel:WORD_1
	v_pk_add_f32 v[98:99], v[98:99], v[102:103]
	v_lshl_add_u64 v[102:103], v[126:127], 0, s[10:11]
	v_pk_add_f32 v[100:101], v[104:105], v[100:101]
	global_store_dwordx4 v[112:113], v[106:109], off offset:2048 nt
	global_store_dwordx4 v[102:103], v[98:101], off offset:16 nt
	s_nop 1
	v_or_b32_e32 v98, 1, v130
	v_ashrrev_i32_e32 v99, 31, v98
	v_lshlrev_b64 v[102:103], 13, v[98:99]
	s_waitcnt vmcnt(31)
	v_cvt_f32_f16_e32 v98, v94
	v_cvt_f32_f16_sdwa v99, v94 dst_sel:DWORD dst_unused:UNUSED_PAD src0_sel:WORD_1
	s_waitcnt vmcnt(30)
	v_cvt_f32_f16_e32 v100, v90
	v_cvt_f32_f16_sdwa v101, v90 dst_sel:DWORD dst_unused:UNUSED_PAD src0_sel:WORD_1
	v_cvt_f32_f16_e32 v94, v95
	v_cvt_f32_f16_sdwa v95, v95 dst_sel:DWORD dst_unused:UNUSED_PAD src0_sel:WORD_1
	v_cvt_f32_f16_e32 v90, v91
	v_cvt_f32_f16_sdwa v91, v91 dst_sel:DWORD dst_unused:UNUSED_PAD src0_sel:WORD_1
	v_pk_add_f32 v[98:99], v[98:99], v[100:101]
	v_pk_add_f32 v[100:101], v[94:95], v[90:91]
	v_cvt_f32_f16_e32 v90, v96
	v_cvt_f32_f16_sdwa v91, v96 dst_sel:DWORD dst_unused:UNUSED_PAD src0_sel:WORD_1
	v_cvt_f32_f16_e32 v94, v92
	v_cvt_f32_f16_sdwa v95, v92 dst_sel:DWORD dst_unused:UNUSED_PAD src0_sel:WORD_1
	v_cvt_f32_f16_e32 v96, v97
	v_cvt_f32_f16_sdwa v97, v97 dst_sel:DWORD dst_unused:UNUSED_PAD src0_sel:WORD_1
	v_cvt_f32_f16_e32 v92, v93
	v_cvt_f32_f16_sdwa v93, v93 dst_sel:DWORD dst_unused:UNUSED_PAD src0_sel:WORD_1
	v_pk_add_f32 v[90:91], v[90:91], v[94:95]
	v_lshl_add_u64 v[94:95], s[58:59], 0, v[102:103]
	v_lshl_add_u64 v[94:95], v[94:95], 0, v[162:163]
	v_pk_add_f32 v[92:93], v[96:97], v[92:93]
	global_store_dwordx4 v[94:95], v[98:101], off nt
	global_store_dwordx4 v[94:95], v[90:93], off offset:16 nt
	s_waitcnt vmcnt(31)
	s_nop 0
	v_cvt_f32_f16_e32 v90, v86
	v_cvt_f32_f16_sdwa v91, v86 dst_sel:DWORD dst_unused:UNUSED_PAD src0_sel:WORD_1
	s_waitcnt vmcnt(30)
	v_cvt_f32_f16_e32 v92, v82
	v_cvt_f32_f16_sdwa v93, v82 dst_sel:DWORD dst_unused:UNUSED_PAD src0_sel:WORD_1
	v_cvt_f32_f16_e32 v86, v87
	v_cvt_f32_f16_sdwa v87, v87 dst_sel:DWORD dst_unused:UNUSED_PAD src0_sel:WORD_1
	v_cvt_f32_f16_e32 v82, v83
	v_cvt_f32_f16_sdwa v83, v83 dst_sel:DWORD dst_unused:UNUSED_PAD src0_sel:WORD_1
	v_pk_add_f32 v[90:91], v[90:91], v[92:93]
	v_pk_add_f32 v[92:93], v[86:87], v[82:83]
	v_cvt_f32_f16_e32 v82, v88
	v_cvt_f32_f16_sdwa v83, v88 dst_sel:DWORD dst_unused:UNUSED_PAD src0_sel:WORD_1
	v_cvt_f32_f16_e32 v86, v84
	v_cvt_f32_f16_sdwa v87, v84 dst_sel:DWORD dst_unused:UNUSED_PAD src0_sel:WORD_1
	v_cvt_f32_f16_e32 v88, v89
	v_cvt_f32_f16_sdwa v89, v89 dst_sel:DWORD dst_unused:UNUSED_PAD src0_sel:WORD_1
	v_cvt_f32_f16_e32 v84, v85
	v_cvt_f32_f16_sdwa v85, v85 dst_sel:DWORD dst_unused:UNUSED_PAD src0_sel:WORD_1
	v_pk_add_f32 v[82:83], v[82:83], v[86:87]
	v_pk_add_f32 v[84:85], v[88:89], v[84:85]
	global_store_dwordx4 v[94:95], v[90:93], off offset:2048 nt
	global_store_dwordx4 v[94:95], v[82:85], off offset:2064 nt
	s_waitcnt vmcnt(31)
	s_nop 0
	v_cvt_f32_f16_e32 v82, v78
	v_cvt_f32_f16_sdwa v83, v78 dst_sel:DWORD dst_unused:UNUSED_PAD src0_sel:WORD_1
	s_waitcnt vmcnt(30)
	v_cvt_f32_f16_e32 v84, v74
	v_cvt_f32_f16_sdwa v85, v74 dst_sel:DWORD dst_unused:UNUSED_PAD src0_sel:WORD_1
	v_cvt_f32_f16_e32 v78, v79
	v_cvt_f32_f16_sdwa v79, v79 dst_sel:DWORD dst_unused:UNUSED_PAD src0_sel:WORD_1
	v_cvt_f32_f16_e32 v74, v75
	v_cvt_f32_f16_sdwa v75, v75 dst_sel:DWORD dst_unused:UNUSED_PAD src0_sel:WORD_1
	v_pk_add_f32 v[82:83], v[82:83], v[84:85]
	v_pk_add_f32 v[84:85], v[78:79], v[74:75]
	v_cvt_f32_f16_e32 v74, v80
	v_cvt_f32_f16_sdwa v75, v80 dst_sel:DWORD dst_unused:UNUSED_PAD src0_sel:WORD_1
	v_cvt_f32_f16_e32 v78, v76
	v_cvt_f32_f16_sdwa v79, v76 dst_sel:DWORD dst_unused:UNUSED_PAD src0_sel:WORD_1
	v_cvt_f32_f16_e32 v80, v81
	v_cvt_f32_f16_sdwa v81, v81 dst_sel:DWORD dst_unused:UNUSED_PAD src0_sel:WORD_1
	v_cvt_f32_f16_e32 v76, v77
	v_cvt_f32_f16_sdwa v77, v77 dst_sel:DWORD dst_unused:UNUSED_PAD src0_sel:WORD_1
	v_pk_add_f32 v[74:75], v[74:75], v[78:79]
	v_lshl_add_u64 v[78:79], v[94:95], 0, s[4:5]
	v_pk_add_f32 v[76:77], v[80:81], v[76:77]
	v_add_co_u32_e32 v80, vcc, s2, v94
	s_nop 1
	v_addc_co_u32_e32 v81, vcc, 0, v95, vcc
	global_store_dwordx4 v[80:81], v[82:85], off nt
	global_store_dwordx4 v[78:79], v[74:77], off offset:16 nt
	s_waitcnt vmcnt(31)
	s_nop 0
	v_cvt_f32_f16_e32 v74, v70
	v_cvt_f32_f16_sdwa v75, v70 dst_sel:DWORD dst_unused:UNUSED_PAD src0_sel:WORD_1
	s_waitcnt vmcnt(30)
	v_cvt_f32_f16_e32 v76, v66
	v_cvt_f32_f16_sdwa v77, v66 dst_sel:DWORD dst_unused:UNUSED_PAD src0_sel:WORD_1
	v_cvt_f32_f16_e32 v70, v71
	v_cvt_f32_f16_sdwa v71, v71 dst_sel:DWORD dst_unused:UNUSED_PAD src0_sel:WORD_1
	v_cvt_f32_f16_e32 v66, v67
	v_cvt_f32_f16_sdwa v67, v67 dst_sel:DWORD dst_unused:UNUSED_PAD src0_sel:WORD_1
	v_pk_add_f32 v[74:75], v[74:75], v[76:77]
	v_pk_add_f32 v[76:77], v[70:71], v[66:67]
	v_cvt_f32_f16_e32 v66, v72
	v_cvt_f32_f16_sdwa v67, v72 dst_sel:DWORD dst_unused:UNUSED_PAD src0_sel:WORD_1
	v_cvt_f32_f16_e32 v70, v68
	v_cvt_f32_f16_sdwa v71, v68 dst_sel:DWORD dst_unused:UNUSED_PAD src0_sel:WORD_1
	v_cvt_f32_f16_e32 v72, v73
	v_cvt_f32_f16_sdwa v73, v73 dst_sel:DWORD dst_unused:UNUSED_PAD src0_sel:WORD_1
	v_cvt_f32_f16_e32 v68, v69
	v_cvt_f32_f16_sdwa v69, v69 dst_sel:DWORD dst_unused:UNUSED_PAD src0_sel:WORD_1
	v_pk_add_f32 v[66:67], v[66:67], v[70:71]
	v_lshl_add_u64 v[70:71], v[94:95], 0, s[10:11]
	v_pk_add_f32 v[68:69], v[72:73], v[68:69]
	global_store_dwordx4 v[80:81], v[74:77], off offset:2048 nt
	global_store_dwordx4 v[70:71], v[66:69], off offset:16 nt
	s_nop 1
	v_or_b32_e32 v66, 2, v130
	v_ashrrev_i32_e32 v67, 31, v66
	v_lshlrev_b64 v[70:71], 13, v[66:67]
	s_waitcnt vmcnt(31)
	v_cvt_f32_f16_e32 v66, v62
	v_cvt_f32_f16_sdwa v67, v62 dst_sel:DWORD dst_unused:UNUSED_PAD src0_sel:WORD_1
	s_waitcnt vmcnt(30)
	v_cvt_f32_f16_e32 v68, v58
	v_cvt_f32_f16_sdwa v69, v58 dst_sel:DWORD dst_unused:UNUSED_PAD src0_sel:WORD_1
	v_cvt_f32_f16_e32 v62, v63
	v_cvt_f32_f16_sdwa v63, v63 dst_sel:DWORD dst_unused:UNUSED_PAD src0_sel:WORD_1
	v_cvt_f32_f16_e32 v58, v59
	v_cvt_f32_f16_sdwa v59, v59 dst_sel:DWORD dst_unused:UNUSED_PAD src0_sel:WORD_1
	v_pk_add_f32 v[66:67], v[66:67], v[68:69]
	v_pk_add_f32 v[68:69], v[62:63], v[58:59]
	v_cvt_f32_f16_e32 v58, v64
	v_cvt_f32_f16_sdwa v59, v64 dst_sel:DWORD dst_unused:UNUSED_PAD src0_sel:WORD_1
	v_cvt_f32_f16_e32 v62, v60
	v_cvt_f32_f16_sdwa v63, v60 dst_sel:DWORD dst_unused:UNUSED_PAD src0_sel:WORD_1
	v_cvt_f32_f16_e32 v64, v65
	v_cvt_f32_f16_sdwa v65, v65 dst_sel:DWORD dst_unused:UNUSED_PAD src0_sel:WORD_1
	v_cvt_f32_f16_e32 v60, v61
	v_cvt_f32_f16_sdwa v61, v61 dst_sel:DWORD dst_unused:UNUSED_PAD src0_sel:WORD_1
	v_pk_add_f32 v[58:59], v[58:59], v[62:63]
	v_lshl_add_u64 v[62:63], s[58:59], 0, v[70:71]
	v_lshl_add_u64 v[62:63], v[62:63], 0, v[162:163]
	v_pk_add_f32 v[60:61], v[64:65], v[60:61]
	global_store_dwordx4 v[62:63], v[66:69], off nt
	global_store_dwordx4 v[62:63], v[58:61], off offset:16 nt
	s_waitcnt vmcnt(31)
	s_nop 0
	v_cvt_f32_f16_e32 v58, v54
	v_cvt_f32_f16_sdwa v59, v54 dst_sel:DWORD dst_unused:UNUSED_PAD src0_sel:WORD_1
	s_waitcnt vmcnt(30)
	v_cvt_f32_f16_e32 v60, v50
	v_cvt_f32_f16_sdwa v61, v50 dst_sel:DWORD dst_unused:UNUSED_PAD src0_sel:WORD_1
	v_cvt_f32_f16_e32 v54, v55
	v_cvt_f32_f16_sdwa v55, v55 dst_sel:DWORD dst_unused:UNUSED_PAD src0_sel:WORD_1
	v_cvt_f32_f16_e32 v50, v51
	v_cvt_f32_f16_sdwa v51, v51 dst_sel:DWORD dst_unused:UNUSED_PAD src0_sel:WORD_1
	v_pk_add_f32 v[58:59], v[58:59], v[60:61]
	v_pk_add_f32 v[60:61], v[54:55], v[50:51]
	v_cvt_f32_f16_e32 v50, v56
	v_cvt_f32_f16_sdwa v51, v56 dst_sel:DWORD dst_unused:UNUSED_PAD src0_sel:WORD_1
	v_cvt_f32_f16_e32 v54, v52
	v_cvt_f32_f16_sdwa v55, v52 dst_sel:DWORD dst_unused:UNUSED_PAD src0_sel:WORD_1
	v_cvt_f32_f16_e32 v56, v57
	v_cvt_f32_f16_sdwa v57, v57 dst_sel:DWORD dst_unused:UNUSED_PAD src0_sel:WORD_1
	v_cvt_f32_f16_e32 v52, v53
	v_cvt_f32_f16_sdwa v53, v53 dst_sel:DWORD dst_unused:UNUSED_PAD src0_sel:WORD_1
	v_pk_add_f32 v[50:51], v[50:51], v[54:55]
	v_pk_add_f32 v[52:53], v[56:57], v[52:53]
	global_store_dwordx4 v[62:63], v[58:61], off offset:2048 nt
	global_store_dwordx4 v[62:63], v[50:53], off offset:2064 nt
	s_waitcnt vmcnt(31)
	s_nop 0
	v_cvt_f32_f16_e32 v50, v46
	v_cvt_f32_f16_sdwa v51, v46 dst_sel:DWORD dst_unused:UNUSED_PAD src0_sel:WORD_1
	s_waitcnt vmcnt(30)
	v_cvt_f32_f16_e32 v52, v42
	v_cvt_f32_f16_sdwa v53, v42 dst_sel:DWORD dst_unused:UNUSED_PAD src0_sel:WORD_1
	v_cvt_f32_f16_e32 v46, v47
	v_cvt_f32_f16_sdwa v47, v47 dst_sel:DWORD dst_unused:UNUSED_PAD src0_sel:WORD_1
	v_cvt_f32_f16_e32 v42, v43
	v_cvt_f32_f16_sdwa v43, v43 dst_sel:DWORD dst_unused:UNUSED_PAD src0_sel:WORD_1
	v_pk_add_f32 v[50:51], v[50:51], v[52:53]
	v_pk_add_f32 v[52:53], v[46:47], v[42:43]
	v_cvt_f32_f16_e32 v42, v48
	v_cvt_f32_f16_sdwa v43, v48 dst_sel:DWORD dst_unused:UNUSED_PAD src0_sel:WORD_1
	v_cvt_f32_f16_e32 v46, v44
	v_cvt_f32_f16_sdwa v47, v44 dst_sel:DWORD dst_unused:UNUSED_PAD src0_sel:WORD_1
	v_cvt_f32_f16_e32 v48, v49
	v_cvt_f32_f16_sdwa v49, v49 dst_sel:DWORD dst_unused:UNUSED_PAD src0_sel:WORD_1
	v_cvt_f32_f16_e32 v44, v45
	v_cvt_f32_f16_sdwa v45, v45 dst_sel:DWORD dst_unused:UNUSED_PAD src0_sel:WORD_1
	v_pk_add_f32 v[42:43], v[42:43], v[46:47]
	v_lshl_add_u64 v[46:47], v[62:63], 0, s[4:5]
	v_pk_add_f32 v[44:45], v[48:49], v[44:45]
	v_add_co_u32_e32 v48, vcc, s2, v62
	s_nop 1
	v_addc_co_u32_e32 v49, vcc, 0, v63, vcc
	global_store_dwordx4 v[48:49], v[50:53], off nt
	global_store_dwordx4 v[46:47], v[42:45], off offset:16 nt
	s_waitcnt vmcnt(31)
	s_nop 0
	v_cvt_f32_f16_e32 v42, v38
	v_cvt_f32_f16_sdwa v43, v38 dst_sel:DWORD dst_unused:UNUSED_PAD src0_sel:WORD_1
	s_waitcnt vmcnt(30)
	v_cvt_f32_f16_e32 v44, v34
	v_cvt_f32_f16_sdwa v45, v34 dst_sel:DWORD dst_unused:UNUSED_PAD src0_sel:WORD_1
	v_cvt_f32_f16_e32 v38, v39
	v_cvt_f32_f16_sdwa v39, v39 dst_sel:DWORD dst_unused:UNUSED_PAD src0_sel:WORD_1
	v_cvt_f32_f16_e32 v34, v35
	v_cvt_f32_f16_sdwa v35, v35 dst_sel:DWORD dst_unused:UNUSED_PAD src0_sel:WORD_1
	v_pk_add_f32 v[42:43], v[42:43], v[44:45]
	v_pk_add_f32 v[44:45], v[38:39], v[34:35]
	v_cvt_f32_f16_e32 v34, v40
	v_cvt_f32_f16_sdwa v35, v40 dst_sel:DWORD dst_unused:UNUSED_PAD src0_sel:WORD_1
	v_cvt_f32_f16_e32 v38, v36
	v_cvt_f32_f16_sdwa v39, v36 dst_sel:DWORD dst_unused:UNUSED_PAD src0_sel:WORD_1
	v_cvt_f32_f16_e32 v40, v41
	v_cvt_f32_f16_sdwa v41, v41 dst_sel:DWORD dst_unused:UNUSED_PAD src0_sel:WORD_1
	v_cvt_f32_f16_e32 v36, v37
	v_cvt_f32_f16_sdwa v37, v37 dst_sel:DWORD dst_unused:UNUSED_PAD src0_sel:WORD_1
	v_pk_add_f32 v[34:35], v[34:35], v[38:39]
	v_lshl_add_u64 v[38:39], v[62:63], 0, s[10:11]
	v_pk_add_f32 v[36:37], v[40:41], v[36:37]
	global_store_dwordx4 v[48:49], v[42:45], off offset:2048 nt
	global_store_dwordx4 v[38:39], v[34:37], off offset:16 nt
	s_nop 1
	v_or_b32_e32 v34, 3, v130
	v_ashrrev_i32_e32 v35, 31, v34
	v_lshlrev_b64 v[38:39], 13, v[34:35]
	s_waitcnt vmcnt(31)
	v_cvt_f32_f16_e32 v34, v30
	v_cvt_f32_f16_sdwa v35, v30 dst_sel:DWORD dst_unused:UNUSED_PAD src0_sel:WORD_1
	s_waitcnt vmcnt(30)
	v_cvt_f32_f16_e32 v36, v26
	v_cvt_f32_f16_sdwa v37, v26 dst_sel:DWORD dst_unused:UNUSED_PAD src0_sel:WORD_1
	v_cvt_f32_f16_e32 v30, v31
	v_cvt_f32_f16_sdwa v31, v31 dst_sel:DWORD dst_unused:UNUSED_PAD src0_sel:WORD_1
	v_cvt_f32_f16_e32 v26, v27
	v_cvt_f32_f16_sdwa v27, v27 dst_sel:DWORD dst_unused:UNUSED_PAD src0_sel:WORD_1
	v_pk_add_f32 v[34:35], v[34:35], v[36:37]
	v_pk_add_f32 v[36:37], v[30:31], v[26:27]
	v_cvt_f32_f16_e32 v26, v32
	v_cvt_f32_f16_sdwa v27, v32 dst_sel:DWORD dst_unused:UNUSED_PAD src0_sel:WORD_1
	v_cvt_f32_f16_e32 v30, v28
	v_cvt_f32_f16_sdwa v31, v28 dst_sel:DWORD dst_unused:UNUSED_PAD src0_sel:WORD_1
	v_cvt_f32_f16_e32 v32, v33
	v_cvt_f32_f16_sdwa v33, v33 dst_sel:DWORD dst_unused:UNUSED_PAD src0_sel:WORD_1
	v_cvt_f32_f16_e32 v28, v29
	v_cvt_f32_f16_sdwa v29, v29 dst_sel:DWORD dst_unused:UNUSED_PAD src0_sel:WORD_1
	v_pk_add_f32 v[26:27], v[26:27], v[30:31]
	v_lshl_add_u64 v[30:31], s[58:59], 0, v[38:39]
	v_lshl_add_u64 v[30:31], v[30:31], 0, v[162:163]
	v_pk_add_f32 v[28:29], v[32:33], v[28:29]
	global_store_dwordx4 v[30:31], v[34:37], off nt
	global_store_dwordx4 v[30:31], v[26:29], off offset:16 nt
	s_waitcnt vmcnt(31)
	s_nop 0
	v_cvt_f32_f16_e32 v26, v22
	v_cvt_f32_f16_sdwa v27, v22 dst_sel:DWORD dst_unused:UNUSED_PAD src0_sel:WORD_1
	s_waitcnt vmcnt(30)
	v_cvt_f32_f16_e32 v28, v18
	v_cvt_f32_f16_sdwa v29, v18 dst_sel:DWORD dst_unused:UNUSED_PAD src0_sel:WORD_1
	v_cvt_f32_f16_e32 v22, v23
	v_cvt_f32_f16_sdwa v23, v23 dst_sel:DWORD dst_unused:UNUSED_PAD src0_sel:WORD_1
	v_cvt_f32_f16_e32 v18, v19
	v_cvt_f32_f16_sdwa v19, v19 dst_sel:DWORD dst_unused:UNUSED_PAD src0_sel:WORD_1
	v_pk_add_f32 v[26:27], v[26:27], v[28:29]
	v_pk_add_f32 v[28:29], v[22:23], v[18:19]
	v_cvt_f32_f16_e32 v18, v24
	v_cvt_f32_f16_sdwa v19, v24 dst_sel:DWORD dst_unused:UNUSED_PAD src0_sel:WORD_1
	v_cvt_f32_f16_e32 v22, v20
	v_cvt_f32_f16_sdwa v23, v20 dst_sel:DWORD dst_unused:UNUSED_PAD src0_sel:WORD_1
	v_cvt_f32_f16_e32 v24, v25
	v_cvt_f32_f16_sdwa v25, v25 dst_sel:DWORD dst_unused:UNUSED_PAD src0_sel:WORD_1
	v_cvt_f32_f16_e32 v20, v21
	v_cvt_f32_f16_sdwa v21, v21 dst_sel:DWORD dst_unused:UNUSED_PAD src0_sel:WORD_1
	v_pk_add_f32 v[18:19], v[18:19], v[22:23]
	v_pk_add_f32 v[20:21], v[24:25], v[20:21]
	global_store_dwordx4 v[30:31], v[26:29], off offset:2048 nt
	global_store_dwordx4 v[30:31], v[18:21], off offset:2064 nt
	s_waitcnt vmcnt(31)
	s_nop 0
	v_cvt_f32_f16_e32 v18, v14
	v_cvt_f32_f16_sdwa v19, v14 dst_sel:DWORD dst_unused:UNUSED_PAD src0_sel:WORD_1
	s_waitcnt vmcnt(30)
	v_cvt_f32_f16_e32 v20, v10
	v_cvt_f32_f16_sdwa v21, v10 dst_sel:DWORD dst_unused:UNUSED_PAD src0_sel:WORD_1
	v_cvt_f32_f16_e32 v14, v15
	v_cvt_f32_f16_sdwa v15, v15 dst_sel:DWORD dst_unused:UNUSED_PAD src0_sel:WORD_1
	v_cvt_f32_f16_e32 v10, v11
	v_cvt_f32_f16_sdwa v11, v11 dst_sel:DWORD dst_unused:UNUSED_PAD src0_sel:WORD_1
	v_pk_add_f32 v[18:19], v[18:19], v[20:21]
	v_pk_add_f32 v[20:21], v[14:15], v[10:11]
	v_cvt_f32_f16_e32 v10, v16
	v_cvt_f32_f16_sdwa v11, v16 dst_sel:DWORD dst_unused:UNUSED_PAD src0_sel:WORD_1
	v_cvt_f32_f16_e32 v14, v12
	v_cvt_f32_f16_sdwa v15, v12 dst_sel:DWORD dst_unused:UNUSED_PAD src0_sel:WORD_1
	v_cvt_f32_f16_e32 v16, v17
	v_cvt_f32_f16_sdwa v17, v17 dst_sel:DWORD dst_unused:UNUSED_PAD src0_sel:WORD_1
	v_cvt_f32_f16_e32 v12, v13
	v_cvt_f32_f16_sdwa v13, v13 dst_sel:DWORD dst_unused:UNUSED_PAD src0_sel:WORD_1
	v_pk_add_f32 v[10:11], v[10:11], v[14:15]
	v_lshl_add_u64 v[14:15], v[30:31], 0, s[4:5]
	v_pk_add_f32 v[12:13], v[16:17], v[12:13]
	v_add_co_u32_e32 v16, vcc, s2, v30
	s_mov_b64 s[2:3], 0
	s_nop 0
	v_addc_co_u32_e32 v17, vcc, 0, v31, vcc
	global_store_dwordx4 v[16:17], v[18:21], off nt
	global_store_dwordx4 v[14:15], v[10:13], off offset:16 nt
	s_waitcnt vmcnt(31)
	s_nop 0
	v_cvt_f32_f16_e32 v10, v6
	v_cvt_f32_f16_sdwa v11, v6 dst_sel:DWORD dst_unused:UNUSED_PAD src0_sel:WORD_1
	s_waitcnt vmcnt(30)
	v_cvt_f32_f16_e32 v12, v2
	v_cvt_f32_f16_sdwa v13, v2 dst_sel:DWORD dst_unused:UNUSED_PAD src0_sel:WORD_1
	v_cvt_f32_f16_e32 v6, v7
	v_cvt_f32_f16_sdwa v7, v7 dst_sel:DWORD dst_unused:UNUSED_PAD src0_sel:WORD_1
	v_cvt_f32_f16_e32 v2, v3
	v_cvt_f32_f16_sdwa v3, v3 dst_sel:DWORD dst_unused:UNUSED_PAD src0_sel:WORD_1
	v_pk_add_f32 v[10:11], v[10:11], v[12:13]
	v_pk_add_f32 v[12:13], v[6:7], v[2:3]
	v_cvt_f32_f16_e32 v2, v8
	v_cvt_f32_f16_sdwa v3, v8 dst_sel:DWORD dst_unused:UNUSED_PAD src0_sel:WORD_1
	v_cvt_f32_f16_e32 v6, v4
	v_cvt_f32_f16_sdwa v7, v4 dst_sel:DWORD dst_unused:UNUSED_PAD src0_sel:WORD_1
	v_cvt_f32_f16_e32 v8, v9
	v_cvt_f32_f16_sdwa v9, v9 dst_sel:DWORD dst_unused:UNUSED_PAD src0_sel:WORD_1
	v_cvt_f32_f16_e32 v4, v5
	v_cvt_f32_f16_sdwa v5, v5 dst_sel:DWORD dst_unused:UNUSED_PAD src0_sel:WORD_1
	v_pk_add_f32 v[2:3], v[2:3], v[6:7]
	v_lshl_add_u64 v[6:7], v[30:31], 0, s[10:11]
	v_pk_add_f32 v[4:5], v[8:9], v[4:5]
	global_store_dwordx4 v[16:17], v[10:13], off offset:2048 nt
	global_store_dwordx4 v[6:7], v[2:5], off offset:16 nt
	s_barrier
